# grid barrier: waiters spin on the top-level generation word (skip per-XCD generation hop), XCD-last no longer bumps per-XCD generation, acquire invalidate issued without waiting for the top-generation
# speedup vs baseline: 1.0029x; 1.0029x over previous
; __device__ __forceinline__ unsigned xb_ld(unsigned* p)              { return __hip_atomic_load(p, __ATOMIC_RELAXED, __HIP_MEMORY_SCOPE_AGENT); }
; __device__ __forceinline__ unsigned xb_add(unsigned* p, unsigned v) { return __hip_atomic_fetch_add(p, v, __ATOMIC_RELAXED, __HIP_MEMORY_SCOPE_AGENT); }
; #define XB_SPIN(cond, bar) do { unsigned _sp = 0; while (cond) { __builtin_amdgcn_s_sleep(1); \
;     if ((++_sp & 255u) == 0u) { if (xb_ld(&(bar)[XB_TMO])) break; if (_sp > XB_SPIN_CAP) { atomicAdd(&(bar)[XB_TMO], 1u); break; } } } } while (0)
; __device__ __forceinline__ void xcd_barrier(const XcdBarrier& b, const bool leader) {
;     ...
;         unsigned nloc = b.st[0], nx = b.st[1];
;         if (nloc == 0u) { xcd_barrier_complete(bar, bx, nloc, nx); b.st[0] = nloc; b.st[1] = nx; }
;         const unsigned old = xb_add(&bar[XB_XSUB(bx)], 1u);
;         const unsigned gen = old / nloc;
;         if (old + 1u == (gen + 1u) * nloc) {
;             __builtin_amdgcn_fence(__ATOMIC_RELEASE, "agent");
;             asm volatile("s_waitcnt vmcnt(0)" ::: "memory");
;             const unsigned og = xb_add(&bar[XB_TOP], 1u);
;             const unsigned tg = og / nx;
;             if (og + 1u == (tg + 1u) * nx) xb_add(&bar[XB_TOPGEN], 1u);
;             else XB_SPIN(xb_ld(&bar[XB_TOPGEN]) == tg, bar);
;             __builtin_amdgcn_fence(__ATOMIC_ACQUIRE, "agent");
;             xb_add(&bar[XB_XGEN(bx)], 1u);
;             asm volatile("s_waitcnt vmcnt(0)" ::: "memory");
;         } else {
;             XB_SPIN(xb_ld(&bar[XB_XGEN(bx)]) == gen, bar);
.LBB0_121:
	s_lshl_b32 s13, s13, 6
	s_add_i32 s20, s13, 0x500
	s_mov_b32 s21, 0
	s_lshl_b64 s[6:7], s[20:21], 2
	s_add_u32 s6, s18, s6
	s_addc_u32 s7, s19, s7
	v_mov_b32_e32 v3, 1
	v_mov_b64_e32 v[6:7], s[6:7]
	flat_atomic_add v3, v[6:7], v3 sc0
	v_cvt_f32_u32_e32 v5, v4
	v_sub_u32_e32 v6, 0, v4
	v_rcp_iflag_f32_e32 v5, v5
	s_nop 0
	v_mul_f32_e32 v5, 0x4f7ffffe, v5
	v_cvt_u32_f32_e32 v5, v5
	v_mul_lo_u32 v6, v6, v5
	v_mul_hi_u32 v6, v5, v6
	v_add_u32_e32 v5, v5, v6
	s_waitcnt vmcnt(0) lgkmcnt(0)
	v_mul_hi_u32 v5, v3, v5
	v_mul_lo_u32 v7, v5, v4
	v_add_u32_e32 v6, 1, v3
	v_sub_u32_e32 v3, v3, v7
	v_add_u32_e32 v8, 1, v5
	v_cmp_ge_u32_e32 vcc, v3, v4
	v_sub_u32_e32 v7, v3, v4
	s_nop 0
	v_cndmask_b32_e32 v5, v5, v8, vcc
	v_cndmask_b32_e32 v3, v3, v7, vcc
	v_add_u32_e32 v7, 1, v5
	v_cmp_ge_u32_e32 vcc, v3, v4
	s_nop 1
	v_cndmask_b32_e32 v3, v5, v7, vcc
	v_mad_u64_u32 v[4:5], s[6:7], v4, v3, v[4:5]
	v_cmp_ne_u32_e32 vcc, v6, v4
	s_and_saveexec_b64 s[6:7], vcc
	s_xor_b64 s[6:7], exec, s[6:7]
	s_cbranch_execz .LBB0_134
	s_add_i32 s20, s13, 0x900
	s_lshl_b64 s[20:21], s[20:21], 2
	s_add_u32 s22, s18, 0x3500
	s_addc_u32 s23, s19, 0
	v_mov_b64_e32 v[4:5], s[22:23]
	flat_load_dword v2, v[4:5] sc1
	s_waitcnt vmcnt(0) lgkmcnt(0)
	v_cmp_eq_u32_e32 vcc, v2, v3
	s_and_saveexec_b64 s[20:21], vcc
	s_cbranch_execz .LBB0_133
	s_mov_b32 s15, 1
	s_mov_b64 s[24:25], 0
	s_branch .LBB0_125

; __device__ __forceinline__ unsigned xb_ld(unsigned* p)              { return __hip_atomic_load(p, __ATOMIC_RELAXED, __HIP_MEMORY_SCOPE_AGENT); }
; __device__ __forceinline__ unsigned xb_add(unsigned* p, unsigned v) { return __hip_atomic_fetch_add(p, v, __ATOMIC_RELAXED, __HIP_MEMORY_SCOPE_AGENT); }
; #define XB_SPIN(cond, bar) do { unsigned _sp = 0; while (cond) { __builtin_amdgcn_s_sleep(1); \
;     if ((++_sp & 255u) == 0u) { if (xb_ld(&(bar)[XB_TMO])) break; if (_sp > XB_SPIN_CAP) { atomicAdd(&(bar)[XB_TMO], 1u); break; } } } } while (0)
; __device__ __forceinline__ void xcd_barrier(const XcdBarrier& b, const bool leader) {
;     ...
;             __builtin_amdgcn_fence(__ATOMIC_RELEASE, "agent");
;             asm volatile("s_waitcnt vmcnt(0)" ::: "memory");
;             const unsigned og = xb_add(&bar[XB_TOP], 1u);
;             const unsigned tg = og / nx;
;             if (og + 1u == (tg + 1u) * nx) xb_add(&bar[XB_TOPGEN], 1u);
;             else XB_SPIN(xb_ld(&bar[XB_TOPGEN]) == tg, bar);
;             __builtin_amdgcn_fence(__ATOMIC_ACQUIRE, "agent");
;             xb_add(&bar[XB_XGEN(bx)], 1u);
;             asm volatile("s_waitcnt vmcnt(0)" ::: "memory");
.LBB0_149:
	s_or_b64 exec, exec, s[6:7]
	s_add_i32 s6, s13, 0x900
	s_mov_b32 s7, 0
	s_lshl_b64 s[6:7], s[6:7], 2
	s_add_u32 s6, s18, s6
	s_addc_u32 s7, s19, s7
	v_mov_b32_e32 v4, 1
	v_mov_b64_e32 v[2:3], s[6:7]
	buffer_inv sc1
	s_waitcnt vmcnt(0)

; __device__ __forceinline__ unsigned xb_ld(unsigned* p)              { return __hip_atomic_load(p, __ATOMIC_RELAXED, __HIP_MEMORY_SCOPE_AGENT); }
; __device__ __forceinline__ unsigned xb_add(unsigned* p, unsigned v) { return __hip_atomic_fetch_add(p, v, __ATOMIC_RELAXED, __HIP_MEMORY_SCOPE_AGENT); }
; #define XB_SPIN(cond, bar) do { unsigned _sp = 0; while (cond) { __builtin_amdgcn_s_sleep(1); \
;     if ((++_sp & 255u) == 0u) { if (xb_ld(&(bar)[XB_TMO])) break; if (_sp > XB_SPIN_CAP) { atomicAdd(&(bar)[XB_TMO], 1u); break; } } } } while (0)
; __device__ __forceinline__ void xcd_barrier(const XcdBarrier& b, const bool leader) {
;     ...
;         unsigned nloc = b.st[0], nx = b.st[1];
;         if (nloc == 0u) { xcd_barrier_complete(bar, bx, nloc, nx); b.st[0] = nloc; b.st[1] = nx; }
;         const unsigned old = xb_add(&bar[XB_XSUB(bx)], 1u);
;         const unsigned gen = old / nloc;
;         if (old + 1u == (gen + 1u) * nloc) {
;             __builtin_amdgcn_fence(__ATOMIC_RELEASE, "agent");
;             asm volatile("s_waitcnt vmcnt(0)" ::: "memory");
;             const unsigned og = xb_add(&bar[XB_TOP], 1u);
;             const unsigned tg = og / nx;
;             if (og + 1u == (tg + 1u) * nx) xb_add(&bar[XB_TOPGEN], 1u);
;             else XB_SPIN(xb_ld(&bar[XB_TOPGEN]) == tg, bar);
;             __builtin_amdgcn_fence(__ATOMIC_ACQUIRE, "agent");
;             xb_add(&bar[XB_XGEN(bx)], 1u);
;             asm volatile("s_waitcnt vmcnt(0)" ::: "memory");
;         } else {
;             XB_SPIN(xb_ld(&bar[XB_XGEN(bx)]) == gen, bar);
.LBB0_239:
	s_lshl_b32 s24, s20, 6
	s_add_i32 s6, s24, 0x500
	s_mov_b32 s7, 0
	s_lshl_b64 s[0:1], s[6:7], 2
	s_add_u32 s0, s4, s0
	s_addc_u32 s1, s5, s1
	v_mov_b32_e32 v1, 1
	v_mov_b64_e32 v[4:5], s[0:1]
	flat_atomic_add v1, v[4:5], v1 sc0
	v_cvt_f32_u32_e32 v3, v2
	v_sub_u32_e32 v4, 0, v2
	v_rcp_iflag_f32_e32 v3, v3
	s_nop 0
	v_mul_f32_e32 v3, 0x4f7ffffe, v3
	v_cvt_u32_f32_e32 v3, v3
	v_mul_lo_u32 v4, v4, v3
	v_mul_hi_u32 v4, v3, v4
	v_add_u32_e32 v3, v3, v4
	s_waitcnt vmcnt(0) lgkmcnt(0)
	v_mul_hi_u32 v3, v1, v3
	v_mul_lo_u32 v5, v3, v2
	v_add_u32_e32 v4, 1, v1
	v_sub_u32_e32 v1, v1, v5
	v_add_u32_e32 v6, 1, v3
	v_cmp_ge_u32_e32 vcc, v1, v2
	v_sub_u32_e32 v5, v1, v2
	s_nop 0
	v_cndmask_b32_e32 v3, v3, v6, vcc
	v_cndmask_b32_e32 v1, v1, v5, vcc
	v_add_u32_e32 v5, 1, v3
	v_cmp_ge_u32_e32 vcc, v1, v2
	s_nop 1
	v_cndmask_b32_e32 v1, v3, v5, vcc
	v_mad_u64_u32 v[2:3], s[0:1], v2, v1, v[2:3]
	v_cmp_ne_u32_e32 vcc, v4, v2
	s_and_saveexec_b64 s[0:1], vcc
	s_xor_b64 s[0:1], exec, s[0:1]
	s_cbranch_execz .LBB0_252
	s_add_i32 s6, s24, 0x900
	s_lshl_b64 s[6:7], s[6:7], 2
	s_add_u32 s8, s4, 0x3500
	s_addc_u32 s9, s5, 0
	v_mov_b64_e32 v[2:3], s[8:9]
	flat_load_dword v0, v[2:3] sc1
	s_waitcnt vmcnt(0) lgkmcnt(0)
	v_cmp_eq_u32_e32 vcc, v0, v1
	s_and_saveexec_b64 s[6:7], vcc
	s_cbranch_execz .LBB0_251
	s_mov_b32 s25, 1
	s_mov_b64 s[10:11], 0
	s_branch .LBB0_243

; __device__ __forceinline__ unsigned xb_ld(unsigned* p)              { return __hip_atomic_load(p, __ATOMIC_RELAXED, __HIP_MEMORY_SCOPE_AGENT); }
; __device__ __forceinline__ unsigned xb_add(unsigned* p, unsigned v) { return __hip_atomic_fetch_add(p, v, __ATOMIC_RELAXED, __HIP_MEMORY_SCOPE_AGENT); }
; #define XB_SPIN(cond, bar) do { unsigned _sp = 0; while (cond) { __builtin_amdgcn_s_sleep(1); \
;     if ((++_sp & 255u) == 0u) { if (xb_ld(&(bar)[XB_TMO])) break; if (_sp > XB_SPIN_CAP) { atomicAdd(&(bar)[XB_TMO], 1u); break; } } } } while (0)
; __device__ __forceinline__ void xcd_barrier(const XcdBarrier& b, const bool leader) {
;     ...
;             __builtin_amdgcn_fence(__ATOMIC_RELEASE, "agent");
;             asm volatile("s_waitcnt vmcnt(0)" ::: "memory");
;             const unsigned og = xb_add(&bar[XB_TOP], 1u);
;             const unsigned tg = og / nx;
;             if (og + 1u == (tg + 1u) * nx) xb_add(&bar[XB_TOPGEN], 1u);
;             else XB_SPIN(xb_ld(&bar[XB_TOPGEN]) == tg, bar);
;             __builtin_amdgcn_fence(__ATOMIC_ACQUIRE, "agent");
;             xb_add(&bar[XB_XGEN(bx)], 1u);
;             asm volatile("s_waitcnt vmcnt(0)" ::: "memory");
.LBB0_267:
	s_or_b64 exec, exec, s[0:1]
	s_add_i32 s0, s24, 0x900
	s_mov_b32 s1, 0
	s_lshl_b64 s[0:1], s[0:1], 2
	s_add_u32 s0, s4, s0
	s_addc_u32 s1, s5, s1
	v_mov_b32_e32 v2, 1
	v_mov_b64_e32 v[0:1], s[0:1]
	buffer_inv sc1
	s_waitcnt vmcnt(0)

; __device__ __forceinline__ unsigned xb_ld(unsigned* p)              { return __hip_atomic_load(p, __ATOMIC_RELAXED, __HIP_MEMORY_SCOPE_AGENT); }
; __device__ __forceinline__ unsigned xb_add(unsigned* p, unsigned v) { return __hip_atomic_fetch_add(p, v, __ATOMIC_RELAXED, __HIP_MEMORY_SCOPE_AGENT); }
; #define XB_SPIN(cond, bar) do { unsigned _sp = 0; while (cond) { __builtin_amdgcn_s_sleep(1); \
;     if ((++_sp & 255u) == 0u) { if (xb_ld(&(bar)[XB_TMO])) break; if (_sp > XB_SPIN_CAP) { atomicAdd(&(bar)[XB_TMO], 1u); break; } } } } while (0)
; __device__ __forceinline__ void xcd_barrier(const XcdBarrier& b, const bool leader) {
;     ...
;             __builtin_amdgcn_fence(__ATOMIC_RELEASE, "agent");
;             asm volatile("s_waitcnt vmcnt(0)" ::: "memory");
;             const unsigned og = xb_add(&bar[XB_TOP], 1u);
;             const unsigned tg = og / nx;
;             if (og + 1u == (tg + 1u) * nx) xb_add(&bar[XB_TOPGEN], 1u);
;             else XB_SPIN(xb_ld(&bar[XB_TOPGEN]) == tg, bar);
;             __builtin_amdgcn_fence(__ATOMIC_ACQUIRE, "agent");
;             xb_add(&bar[XB_XGEN(bx)], 1u);
;             asm volatile("s_waitcnt vmcnt(0)" ::: "memory");
.LBB0_270:
	s_or_b64 exec, exec, s[4:5]
	s_add_i32 s30, s24, 0x900
	s_lshl_b64 s[4:5], s[30:31], 2
	s_add_u32 s2, s2, s4
	s_addc_u32 s3, s3, s5
	v_mov_b64_e32 v[2:3], s[2:3]
	buffer_inv sc1
	s_waitcnt vmcnt(0)

; __device__ __forceinline__ unsigned xb_ld(unsigned* p)              { return __hip_atomic_load(p, __ATOMIC_RELAXED, __HIP_MEMORY_SCOPE_AGENT); }
; __device__ __forceinline__ unsigned xb_add(unsigned* p, unsigned v) { return __hip_atomic_fetch_add(p, v, __ATOMIC_RELAXED, __HIP_MEMORY_SCOPE_AGENT); }
; #define XB_SPIN(cond, bar) do { unsigned _sp = 0; while (cond) { __builtin_amdgcn_s_sleep(1); \
;     if ((++_sp & 255u) == 0u) { if (xb_ld(&(bar)[XB_TMO])) break; if (_sp > XB_SPIN_CAP) { atomicAdd(&(bar)[XB_TMO], 1u); break; } } } } while (0)
; __device__ __forceinline__ void xcd_barrier(const XcdBarrier& b, const bool leader) {
;     ...
;         unsigned nloc = b.st[0], nx = b.st[1];
;         if (nloc == 0u) { xcd_barrier_complete(bar, bx, nloc, nx); b.st[0] = nloc; b.st[1] = nx; }
;         const unsigned old = xb_add(&bar[XB_XSUB(bx)], 1u);
;         const unsigned gen = old / nloc;
;         if (old + 1u == (gen + 1u) * nloc) {
;             __builtin_amdgcn_fence(__ATOMIC_RELEASE, "agent");
;             asm volatile("s_waitcnt vmcnt(0)" ::: "memory");
;             const unsigned og = xb_add(&bar[XB_TOP], 1u);
;             const unsigned tg = og / nx;
;             if (og + 1u == (tg + 1u) * nx) xb_add(&bar[XB_TOPGEN], 1u);
;             else XB_SPIN(xb_ld(&bar[XB_TOPGEN]) == tg, bar);
;             __builtin_amdgcn_fence(__ATOMIC_ACQUIRE, "agent");
;             xb_add(&bar[XB_XGEN(bx)], 1u);
;             asm volatile("s_waitcnt vmcnt(0)" ::: "memory");
;         } else {
;             XB_SPIN(xb_ld(&bar[XB_XGEN(bx)]) == gen, bar);
.LBB0_339:
	s_lshl_b32 s27, s22, 6
	s_add_i32 s30, s27, 0x500
	s_lshl_b64 s[6:7], s[30:31], 2
	s_add_u32 s6, s4, s6
	s_addc_u32 s7, s5, s7
	v_mov_b64_e32 v[4:5], s[6:7]
	flat_atomic_add v4, v[4:5], v206 sc0
	v_cvt_f32_u32_e32 v3, v2
	v_sub_u32_e32 v5, 0, v2
	v_rcp_iflag_f32_e32 v3, v3
	s_nop 0
	v_mul_f32_e32 v3, 0x4f7ffffe, v3
	v_cvt_u32_f32_e32 v3, v3
	v_mul_lo_u32 v5, v5, v3
	v_mul_hi_u32 v5, v3, v5
	v_add_u32_e32 v3, v3, v5
	s_waitcnt vmcnt(0) lgkmcnt(0)
	v_mul_hi_u32 v3, v4, v3
	v_mul_lo_u32 v5, v3, v2
	v_sub_u32_e32 v5, v4, v5
	v_cmp_ge_u32_e32 vcc, v5, v2
	v_add_u32_e32 v6, 1, v3
	s_nop 0
	v_cndmask_b32_e32 v3, v3, v6, vcc
	v_sub_u32_e32 v6, v5, v2
	v_cndmask_b32_e32 v5, v5, v6, vcc
	v_cmp_ge_u32_e32 vcc, v5, v2
	v_add_u32_e32 v5, 1, v3
	v_add_u32_e32 v6, 1, v4
	v_cndmask_b32_e32 v3, v3, v5, vcc
	v_mad_u64_u32 v[4:5], s[6:7], v2, v3, v[2:3]
	v_cmp_ne_u32_e32 vcc, v6, v4
	s_and_saveexec_b64 s[6:7], vcc
	s_xor_b64 s[6:7], exec, s[6:7]
	s_cbranch_execz .LBB0_352
	s_add_i32 s30, s27, 0x900
	s_lshl_b64 s[8:9], s[30:31], 2
	s_add_u32 s10, s4, 0x3500
	s_addc_u32 s11, s5, 0
	v_mov_b64_e32 v[4:5], s[10:11]
	flat_load_dword v0, v[4:5] sc1
	s_waitcnt vmcnt(0) lgkmcnt(0)
	v_cmp_eq_u32_e32 vcc, v0, v3
	s_and_saveexec_b64 s[8:9], vcc
	s_cbranch_execz .LBB0_351
	s_mov_b32 s28, 1
	s_mov_b64 s[12:13], 0
	s_branch .LBB0_343

; __device__ __forceinline__ unsigned xb_ld(unsigned* p)              { return __hip_atomic_load(p, __ATOMIC_RELAXED, __HIP_MEMORY_SCOPE_AGENT); }
; __device__ __forceinline__ unsigned xb_add(unsigned* p, unsigned v) { return __hip_atomic_fetch_add(p, v, __ATOMIC_RELAXED, __HIP_MEMORY_SCOPE_AGENT); }
; #define XB_SPIN(cond, bar) do { unsigned _sp = 0; while (cond) { __builtin_amdgcn_s_sleep(1); \
;     if ((++_sp & 255u) == 0u) { if (xb_ld(&(bar)[XB_TMO])) break; if (_sp > XB_SPIN_CAP) { atomicAdd(&(bar)[XB_TMO], 1u); break; } } } } while (0)
; __device__ __forceinline__ void xcd_barrier(const XcdBarrier& b, const bool leader) {
;     ...
;             __builtin_amdgcn_fence(__ATOMIC_RELEASE, "agent");
;             asm volatile("s_waitcnt vmcnt(0)" ::: "memory");
;             const unsigned og = xb_add(&bar[XB_TOP], 1u);
;             const unsigned tg = og / nx;
;             if (og + 1u == (tg + 1u) * nx) xb_add(&bar[XB_TOPGEN], 1u);
;             else XB_SPIN(xb_ld(&bar[XB_TOPGEN]) == tg, bar);
;             __builtin_amdgcn_fence(__ATOMIC_ACQUIRE, "agent");
;             xb_add(&bar[XB_XGEN(bx)], 1u);
;             asm volatile("s_waitcnt vmcnt(0)" ::: "memory");
.LBB0_367:
	s_or_b64 exec, exec, s[6:7]
	s_add_i32 s30, s27, 0x900
	s_lshl_b64 s[6:7], s[30:31], 2
	s_add_u32 s4, s4, s6
	s_addc_u32 s5, s5, s7
	v_mov_b64_e32 v[2:3], s[4:5]
	buffer_inv sc1
	s_waitcnt vmcnt(0)

; __device__ __forceinline__ unsigned xb_ld(unsigned* p)              { return __hip_atomic_load(p, __ATOMIC_RELAXED, __HIP_MEMORY_SCOPE_AGENT); }
; __device__ __forceinline__ unsigned xb_add(unsigned* p, unsigned v) { return __hip_atomic_fetch_add(p, v, __ATOMIC_RELAXED, __HIP_MEMORY_SCOPE_AGENT); }
; #define XB_SPIN(cond, bar) do { unsigned _sp = 0; while (cond) { __builtin_amdgcn_s_sleep(1); \
;     if ((++_sp & 255u) == 0u) { if (xb_ld(&(bar)[XB_TMO])) break; if (_sp > XB_SPIN_CAP) { atomicAdd(&(bar)[XB_TMO], 1u); break; } } } } while (0)
; __device__ __forceinline__ void xcd_barrier(const XcdBarrier& b, const bool leader) {
;     ...
;         unsigned nloc = b.st[0], nx = b.st[1];
;         if (nloc == 0u) { xcd_barrier_complete(bar, bx, nloc, nx); b.st[0] = nloc; b.st[1] = nx; }
;         const unsigned old = xb_add(&bar[XB_XSUB(bx)], 1u);
;         const unsigned gen = old / nloc;
;         if (old + 1u == (gen + 1u) * nloc) {
;             __builtin_amdgcn_fence(__ATOMIC_RELEASE, "agent");
;             asm volatile("s_waitcnt vmcnt(0)" ::: "memory");
;             const unsigned og = xb_add(&bar[XB_TOP], 1u);
;             const unsigned tg = og / nx;
;             if (og + 1u == (tg + 1u) * nx) xb_add(&bar[XB_TOPGEN], 1u);
;             else XB_SPIN(xb_ld(&bar[XB_TOPGEN]) == tg, bar);
;             __builtin_amdgcn_fence(__ATOMIC_ACQUIRE, "agent");
;             xb_add(&bar[XB_XGEN(bx)], 1u);
;             asm volatile("s_waitcnt vmcnt(0)" ::: "memory");
;         } else {
;             XB_SPIN(xb_ld(&bar[XB_XGEN(bx)]) == gen, bar);
.LBB0_420:
	s_lshl_b32 s25, s20, 6
	s_add_i32 s30, s25, 0x500
	s_lshl_b64 s[4:5], s[30:31], 2
	s_add_u32 s4, s2, s4
	s_addc_u32 s5, s3, s5
	v_mov_b64_e32 v[4:5], s[4:5]
	flat_atomic_add v4, v[4:5], v206 sc0
	v_cvt_f32_u32_e32 v3, v2
	v_sub_u32_e32 v5, 0, v2
	v_rcp_iflag_f32_e32 v3, v3
	s_nop 0
	v_mul_f32_e32 v3, 0x4f7ffffe, v3
	v_cvt_u32_f32_e32 v3, v3
	v_mul_lo_u32 v5, v5, v3
	v_mul_hi_u32 v5, v3, v5
	v_add_u32_e32 v3, v3, v5
	s_waitcnt vmcnt(0) lgkmcnt(0)
	v_mul_hi_u32 v3, v4, v3
	v_mul_lo_u32 v5, v3, v2
	v_sub_u32_e32 v5, v4, v5
	v_cmp_ge_u32_e32 vcc, v5, v2
	v_add_u32_e32 v6, 1, v3
	s_nop 0
	v_cndmask_b32_e32 v3, v3, v6, vcc
	v_sub_u32_e32 v6, v5, v2
	v_cndmask_b32_e32 v5, v5, v6, vcc
	v_cmp_ge_u32_e32 vcc, v5, v2
	v_add_u32_e32 v5, 1, v3
	v_add_u32_e32 v6, 1, v4
	v_cndmask_b32_e32 v3, v3, v5, vcc
	v_mad_u64_u32 v[4:5], s[4:5], v2, v3, v[2:3]
	v_cmp_ne_u32_e32 vcc, v6, v4
	s_and_saveexec_b64 s[4:5], vcc
	s_xor_b64 s[4:5], exec, s[4:5]
	s_cbranch_execz .LBB0_433
	s_add_i32 s30, s25, 0x900
	s_lshl_b64 s[6:7], s[30:31], 2
	s_add_u32 s8, s2, 0x3500
	s_addc_u32 s9, s3, 0
	v_mov_b64_e32 v[4:5], s[8:9]
	flat_load_dword v0, v[4:5] sc1
	s_waitcnt vmcnt(0) lgkmcnt(0)
	v_cmp_eq_u32_e32 vcc, v0, v3
	s_and_saveexec_b64 s[6:7], vcc
	s_cbranch_execz .LBB0_432
	s_mov_b32 s26, 1
	s_mov_b64 s[10:11], 0
	s_branch .LBB0_424

; __device__ __forceinline__ unsigned xb_ld(unsigned* p)              { return __hip_atomic_load(p, __ATOMIC_RELAXED, __HIP_MEMORY_SCOPE_AGENT); }
; __device__ __forceinline__ unsigned xb_add(unsigned* p, unsigned v) { return __hip_atomic_fetch_add(p, v, __ATOMIC_RELAXED, __HIP_MEMORY_SCOPE_AGENT); }
; #define XB_SPIN(cond, bar) do { unsigned _sp = 0; while (cond) { __builtin_amdgcn_s_sleep(1); \
;     if ((++_sp & 255u) == 0u) { if (xb_ld(&(bar)[XB_TMO])) break; if (_sp > XB_SPIN_CAP) { atomicAdd(&(bar)[XB_TMO], 1u); break; } } } } while (0)
; __device__ __forceinline__ void xcd_barrier(const XcdBarrier& b, const bool leader) {
;     ...
;             __builtin_amdgcn_fence(__ATOMIC_RELEASE, "agent");
;             asm volatile("s_waitcnt vmcnt(0)" ::: "memory");
;             const unsigned og = xb_add(&bar[XB_TOP], 1u);
;             const unsigned tg = og / nx;
;             if (og + 1u == (tg + 1u) * nx) xb_add(&bar[XB_TOPGEN], 1u);
;             else XB_SPIN(xb_ld(&bar[XB_TOPGEN]) == tg, bar);
;             __builtin_amdgcn_fence(__ATOMIC_ACQUIRE, "agent");
;             xb_add(&bar[XB_XGEN(bx)], 1u);
;             asm volatile("s_waitcnt vmcnt(0)" ::: "memory");
.LBB0_448:
	s_or_b64 exec, exec, s[4:5]
	s_add_i32 s30, s25, 0x900
	s_lshl_b64 s[4:5], s[30:31], 2
	s_add_u32 s2, s2, s4
	s_addc_u32 s3, s3, s5
	v_mov_b64_e32 v[2:3], s[2:3]
	buffer_inv sc1
	s_waitcnt vmcnt(0)

; __device__ __forceinline__ unsigned xb_ld(unsigned* p)              { return __hip_atomic_load(p, __ATOMIC_RELAXED, __HIP_MEMORY_SCOPE_AGENT); }
; __device__ __forceinline__ unsigned xb_add(unsigned* p, unsigned v) { return __hip_atomic_fetch_add(p, v, __ATOMIC_RELAXED, __HIP_MEMORY_SCOPE_AGENT); }
; #define XB_SPIN(cond, bar) do { unsigned _sp = 0; while (cond) { __builtin_amdgcn_s_sleep(1); \
;     if ((++_sp & 255u) == 0u) { if (xb_ld(&(bar)[XB_TMO])) break; if (_sp > XB_SPIN_CAP) { atomicAdd(&(bar)[XB_TMO], 1u); break; } } } } while (0)
; __device__ __forceinline__ void xcd_barrier(const XcdBarrier& b, const bool leader) {
;     ...
;         unsigned nloc = b.st[0], nx = b.st[1];
;         if (nloc == 0u) { xcd_barrier_complete(bar, bx, nloc, nx); b.st[0] = nloc; b.st[1] = nx; }
;         const unsigned old = xb_add(&bar[XB_XSUB(bx)], 1u);
;         const unsigned gen = old / nloc;
;         if (old + 1u == (gen + 1u) * nloc) {
;             __builtin_amdgcn_fence(__ATOMIC_RELEASE, "agent");
;             asm volatile("s_waitcnt vmcnt(0)" ::: "memory");
;             const unsigned og = xb_add(&bar[XB_TOP], 1u);
;             const unsigned tg = og / nx;
;             if (og + 1u == (tg + 1u) * nx) xb_add(&bar[XB_TOPGEN], 1u);
;             else XB_SPIN(xb_ld(&bar[XB_TOPGEN]) == tg, bar);
;             __builtin_amdgcn_fence(__ATOMIC_ACQUIRE, "agent");
;             xb_add(&bar[XB_XGEN(bx)], 1u);
;             asm volatile("s_waitcnt vmcnt(0)" ::: "memory");
;         } else {
;             XB_SPIN(xb_ld(&bar[XB_XGEN(bx)]) == gen, bar);
.LBB0_641:
	s_lshl_b32 s28, s24, 6
	s_add_i32 s30, s28, 0x500
	s_lshl_b64 s[6:7], s[30:31], 2
	s_add_u32 s6, s4, s6
	s_addc_u32 s7, s5, s7
	v_mov_b64_e32 v[4:5], s[6:7]
	flat_atomic_add v4, v[4:5], v206 sc0
	v_cvt_f32_u32_e32 v3, v2
	v_sub_u32_e32 v5, 0, v2
	v_rcp_iflag_f32_e32 v3, v3
	s_nop 0
	v_mul_f32_e32 v3, 0x4f7ffffe, v3
	v_cvt_u32_f32_e32 v3, v3
	v_mul_lo_u32 v5, v5, v3
	v_mul_hi_u32 v5, v3, v5
	v_add_u32_e32 v3, v3, v5
	s_waitcnt vmcnt(0) lgkmcnt(0)
	v_mul_hi_u32 v3, v4, v3
	v_mul_lo_u32 v5, v3, v2
	v_sub_u32_e32 v5, v4, v5
	v_cmp_ge_u32_e32 vcc, v5, v2
	v_add_u32_e32 v6, 1, v3
	s_nop 0
	v_cndmask_b32_e32 v3, v3, v6, vcc
	v_sub_u32_e32 v6, v5, v2
	v_cndmask_b32_e32 v5, v5, v6, vcc
	v_cmp_ge_u32_e32 vcc, v5, v2
	v_add_u32_e32 v5, 1, v3
	v_add_u32_e32 v6, 1, v4
	v_cndmask_b32_e32 v3, v3, v5, vcc
	v_mad_u64_u32 v[4:5], s[6:7], v2, v3, v[2:3]
	v_cmp_ne_u32_e32 vcc, v6, v4
	s_and_saveexec_b64 s[6:7], vcc
	s_xor_b64 s[6:7], exec, s[6:7]
	s_cbranch_execz .LBB0_654
	s_add_i32 s30, s28, 0x900
	s_lshl_b64 s[8:9], s[30:31], 2
	s_add_u32 s10, s4, 0x3500
	s_addc_u32 s11, s5, 0
	v_mov_b64_e32 v[4:5], s[10:11]
	flat_load_dword v0, v[4:5] sc1
	s_waitcnt vmcnt(0) lgkmcnt(0)
	v_cmp_eq_u32_e32 vcc, v0, v3
	s_and_saveexec_b64 s[8:9], vcc
	s_cbranch_execz .LBB0_653
	s_mov_b32 s29, 1
	s_mov_b64 s[12:13], 0
	s_branch .LBB0_645

; __device__ __forceinline__ unsigned xb_ld(unsigned* p)              { return __hip_atomic_load(p, __ATOMIC_RELAXED, __HIP_MEMORY_SCOPE_AGENT); }
; __device__ __forceinline__ unsigned xb_add(unsigned* p, unsigned v) { return __hip_atomic_fetch_add(p, v, __ATOMIC_RELAXED, __HIP_MEMORY_SCOPE_AGENT); }
; #define XB_SPIN(cond, bar) do { unsigned _sp = 0; while (cond) { __builtin_amdgcn_s_sleep(1); \
;     if ((++_sp & 255u) == 0u) { if (xb_ld(&(bar)[XB_TMO])) break; if (_sp > XB_SPIN_CAP) { atomicAdd(&(bar)[XB_TMO], 1u); break; } } } } while (0)
; __device__ __forceinline__ void xcd_barrier(const XcdBarrier& b, const bool leader) {
;     ...
;             __builtin_amdgcn_fence(__ATOMIC_RELEASE, "agent");
;             asm volatile("s_waitcnt vmcnt(0)" ::: "memory");
;             const unsigned og = xb_add(&bar[XB_TOP], 1u);
;             const unsigned tg = og / nx;
;             if (og + 1u == (tg + 1u) * nx) xb_add(&bar[XB_TOPGEN], 1u);
;             else XB_SPIN(xb_ld(&bar[XB_TOPGEN]) == tg, bar);
;             __builtin_amdgcn_fence(__ATOMIC_ACQUIRE, "agent");
;             xb_add(&bar[XB_XGEN(bx)], 1u);
;             asm volatile("s_waitcnt vmcnt(0)" ::: "memory");
.LBB0_669:
	s_or_b64 exec, exec, s[6:7]
	s_add_i32 s30, s28, 0x900
	s_lshl_b64 s[6:7], s[30:31], 2
	s_add_u32 s4, s4, s6
	s_addc_u32 s5, s5, s7
	v_mov_b64_e32 v[2:3], s[4:5]
	buffer_inv sc1
	s_waitcnt vmcnt(0)

; __device__ __forceinline__ unsigned xb_ld(unsigned* p)              { return __hip_atomic_load(p, __ATOMIC_RELAXED, __HIP_MEMORY_SCOPE_AGENT); }
; __device__ __forceinline__ unsigned xb_add(unsigned* p, unsigned v) { return __hip_atomic_fetch_add(p, v, __ATOMIC_RELAXED, __HIP_MEMORY_SCOPE_AGENT); }
; #define XB_SPIN(cond, bar) do { unsigned _sp = 0; while (cond) { __builtin_amdgcn_s_sleep(1); \
;     if ((++_sp & 255u) == 0u) { if (xb_ld(&(bar)[XB_TMO])) break; if (_sp > XB_SPIN_CAP) { atomicAdd(&(bar)[XB_TMO], 1u); break; } } } } while (0)
; __device__ __forceinline__ void xcd_barrier(const XcdBarrier& b, const bool leader) {
;     ...
;         unsigned nloc = b.st[0], nx = b.st[1];
;         if (nloc == 0u) { xcd_barrier_complete(bar, bx, nloc, nx); b.st[0] = nloc; b.st[1] = nx; }
;         const unsigned old = xb_add(&bar[XB_XSUB(bx)], 1u);
;         const unsigned gen = old / nloc;
;         if (old + 1u == (gen + 1u) * nloc) {
;             __builtin_amdgcn_fence(__ATOMIC_RELEASE, "agent");
;             asm volatile("s_waitcnt vmcnt(0)" ::: "memory");
;             const unsigned og = xb_add(&bar[XB_TOP], 1u);
;             const unsigned tg = og / nx;
;             if (og + 1u == (tg + 1u) * nx) xb_add(&bar[XB_TOPGEN], 1u);
;             else XB_SPIN(xb_ld(&bar[XB_TOPGEN]) == tg, bar);
;             __builtin_amdgcn_fence(__ATOMIC_ACQUIRE, "agent");
;             xb_add(&bar[XB_XGEN(bx)], 1u);
;             asm volatile("s_waitcnt vmcnt(0)" ::: "memory");
;         } else {
;             XB_SPIN(xb_ld(&bar[XB_XGEN(bx)]) == gen, bar);
.LBB0_729:
	s_lshl_b32 s24, s20, 6
	s_add_i32 s30, s24, 0x500
	s_lshl_b64 s[4:5], s[30:31], 2
	s_add_u32 s4, s2, s4
	s_addc_u32 s5, s3, s5
	v_mov_b64_e32 v[4:5], s[4:5]
	flat_atomic_add v4, v[4:5], v206 sc0
	v_cvt_f32_u32_e32 v3, v2
	v_sub_u32_e32 v5, 0, v2
	v_rcp_iflag_f32_e32 v3, v3
	s_nop 0
	v_mul_f32_e32 v3, 0x4f7ffffe, v3
	v_cvt_u32_f32_e32 v3, v3
	v_mul_lo_u32 v5, v5, v3
	v_mul_hi_u32 v5, v3, v5
	v_add_u32_e32 v3, v3, v5
	s_waitcnt vmcnt(0) lgkmcnt(0)
	v_mul_hi_u32 v3, v4, v3
	v_mul_lo_u32 v5, v3, v2
	v_sub_u32_e32 v5, v4, v5
	v_cmp_ge_u32_e32 vcc, v5, v2
	v_add_u32_e32 v6, 1, v3
	s_nop 0
	v_cndmask_b32_e32 v3, v3, v6, vcc
	v_sub_u32_e32 v6, v5, v2
	v_cndmask_b32_e32 v5, v5, v6, vcc
	v_cmp_ge_u32_e32 vcc, v5, v2
	v_add_u32_e32 v5, 1, v3
	v_add_u32_e32 v6, 1, v4
	v_cndmask_b32_e32 v3, v3, v5, vcc
	v_mad_u64_u32 v[4:5], s[4:5], v2, v3, v[2:3]
	v_cmp_ne_u32_e32 vcc, v6, v4
	s_and_saveexec_b64 s[4:5], vcc
	s_xor_b64 s[4:5], exec, s[4:5]
	s_cbranch_execz .LBB0_742
	s_add_i32 s30, s24, 0x900
	s_lshl_b64 s[6:7], s[30:31], 2
	s_add_u32 s8, s2, 0x3500
	s_addc_u32 s9, s3, 0
	v_mov_b64_e32 v[4:5], s[8:9]
	flat_load_dword v0, v[4:5] sc1
	s_waitcnt vmcnt(0) lgkmcnt(0)
	v_cmp_eq_u32_e32 vcc, v0, v3
	s_and_saveexec_b64 s[6:7], vcc
	s_cbranch_execz .LBB0_741
	s_mov_b32 s25, 1
	s_mov_b64 s[10:11], 0
	s_branch .LBB0_733

; __device__ __forceinline__ unsigned xb_ld(unsigned* p)              { return __hip_atomic_load(p, __ATOMIC_RELAXED, __HIP_MEMORY_SCOPE_AGENT); }
; __device__ __forceinline__ unsigned xb_add(unsigned* p, unsigned v) { return __hip_atomic_fetch_add(p, v, __ATOMIC_RELAXED, __HIP_MEMORY_SCOPE_AGENT); }
; #define XB_SPIN(cond, bar) do { unsigned _sp = 0; while (cond) { __builtin_amdgcn_s_sleep(1); \
;     if ((++_sp & 255u) == 0u) { if (xb_ld(&(bar)[XB_TMO])) break; if (_sp > XB_SPIN_CAP) { atomicAdd(&(bar)[XB_TMO], 1u); break; } } } } while (0)
; __device__ __forceinline__ void xcd_barrier(const XcdBarrier& b, const bool leader) {
;     ...
;         unsigned nloc = b.st[0], nx = b.st[1];
;         if (nloc == 0u) { xcd_barrier_complete(bar, bx, nloc, nx); b.st[0] = nloc; b.st[1] = nx; }
;         const unsigned old = xb_add(&bar[XB_XSUB(bx)], 1u);
;         const unsigned gen = old / nloc;
;         if (old + 1u == (gen + 1u) * nloc) {
;             __builtin_amdgcn_fence(__ATOMIC_RELEASE, "agent");
;             asm volatile("s_waitcnt vmcnt(0)" ::: "memory");
;             const unsigned og = xb_add(&bar[XB_TOP], 1u);
;             const unsigned tg = og / nx;
;             if (og + 1u == (tg + 1u) * nx) xb_add(&bar[XB_TOPGEN], 1u);
;             else XB_SPIN(xb_ld(&bar[XB_TOPGEN]) == tg, bar);
;             __builtin_amdgcn_fence(__ATOMIC_ACQUIRE, "agent");
;             xb_add(&bar[XB_XGEN(bx)], 1u);
;             asm volatile("s_waitcnt vmcnt(0)" ::: "memory");
;         } else {
;             XB_SPIN(xb_ld(&bar[XB_XGEN(bx)]) == gen, bar);
.LBB0_1470:
	s_lshl_b32 s24, s20, 6
	s_add_i32 s30, s24, 0x500
	s_lshl_b64 s[4:5], s[30:31], 2
	s_add_u32 s4, s2, s4
	s_addc_u32 s5, s3, s5
	v_mov_b64_e32 v[4:5], s[4:5]
	flat_atomic_add v3, v[4:5], v206 sc0
	v_cvt_f32_u32_e32 v4, v2
	v_sub_u32_e32 v5, 0, v2
	v_rcp_iflag_f32_e32 v4, v4
	s_nop 0
	v_mul_f32_e32 v4, 0x4f7ffffe, v4
	v_cvt_u32_f32_e32 v4, v4
	v_mul_lo_u32 v5, v5, v4
	v_mul_hi_u32 v5, v4, v5
	v_add_u32_e32 v4, v4, v5
	s_waitcnt vmcnt(0) lgkmcnt(0)
	v_mul_hi_u32 v4, v3, v4
	v_mul_lo_u32 v5, v4, v2
	v_add_u32_e32 v6, 1, v3
	v_sub_u32_e32 v3, v3, v5
	v_add_u32_e32 v7, 1, v4
	v_cmp_ge_u32_e32 vcc, v3, v2
	v_sub_u32_e32 v5, v3, v2
	s_nop 0
	v_cndmask_b32_e32 v4, v4, v7, vcc
	v_cndmask_b32_e32 v3, v3, v5, vcc
	v_add_u32_e32 v5, 1, v4
	v_cmp_ge_u32_e32 vcc, v3, v2
	s_nop 1
	v_cndmask_b32_e32 v3, v4, v5, vcc
	v_mad_u64_u32 v[4:5], s[4:5], v2, v3, v[2:3]
	v_cmp_ne_u32_e32 vcc, v6, v4
	s_and_saveexec_b64 s[4:5], vcc
	s_xor_b64 s[4:5], exec, s[4:5]
	s_cbranch_execz .LBB0_1483
	s_add_i32 s30, s24, 0x900
	s_lshl_b64 s[6:7], s[30:31], 2
	s_add_u32 s8, s2, 0x3500
	s_addc_u32 s9, s3, 0
	v_mov_b64_e32 v[4:5], s[8:9]
	flat_load_dword v0, v[4:5] sc1
	s_waitcnt vmcnt(0) lgkmcnt(0)
	v_cmp_eq_u32_e32 vcc, v0, v3
	s_and_saveexec_b64 s[6:7], vcc
	s_cbranch_execz .LBB0_1482
	s_mov_b32 s25, 1
	s_mov_b64 s[10:11], 0
	s_branch .LBB0_1474
